# grid_barrier_acquire_issued_at_arrival_overlapping_poll
# speedup vs baseline: 1.0079x; 1.0079x over previous
.LBB0_209:
	s_or_b64 exec, exec, s[4:5]
	buffer_inv sc1
	s_waitcnt vmcnt(1)
	v_readfirstlane_b32 s2, v5
	v_sub_u32_e32 v6, 0, v4
	s_nop 0
	v_add_u32_e32 v5, s2, v3
	v_cvt_f32_u32_e32 v3, v4
	v_rcp_iflag_f32_e32 v3, v3
	s_nop 0
	v_mul_f32_e32 v3, 0x4f7ffffe, v3
	v_cvt_u32_f32_e32 v3, v3
	v_mul_lo_u32 v6, v6, v3
	v_mul_hi_u32 v6, v3, v6
	v_add_u32_e32 v3, v3, v6
	v_mul_hi_u32 v3, v5, v3
	v_mul_lo_u32 v6, v3, v4
	v_sub_u32_e32 v6, v5, v6
	v_cmp_ge_u32_e32 vcc, v6, v4
	v_add_u32_e32 v7, 1, v3
	s_nop 0
	v_cndmask_b32_e32 v3, v3, v7, vcc
	v_sub_u32_e32 v7, v6, v4
	v_cndmask_b32_e32 v6, v6, v7, vcc
	v_cmp_ge_u32_e32 vcc, v6, v4
	v_add_u32_e32 v6, 1, v3
	s_nop 0
	v_cndmask_b32_e32 v3, v3, v6, vcc
	v_add_u32_e32 v6, 1, v5
	v_mad_u64_u32 v[4:5], s[2:3], v4, v3, v[4:5]
	v_cmp_ne_u32_e32 vcc, v6, v4
	s_and_saveexec_b64 s[2:3], vcc
	s_xor_b64 s[2:3], exec, s[2:3]
	v_readlane_b32 s37, v253, 9
	s_cbranch_execz .LBB0_223
	s_waitcnt lgkmcnt(0)
	v_mov_b32_e32 v2, 0x2000
	global_load_dword v2, v2, s[0:1] offset:1024 sc1
	s_add_u32 s6, s0, 0x2400
	s_addc_u32 s7, s1, 0
	s_waitcnt vmcnt(0)
	v_cmp_eq_u32_e32 vcc, v2, v3
	s_and_saveexec_b64 s[4:5], vcc
	s_cbranch_execz .LBB0_222
	s_mov_b32 s18, 1
	s_mov_b64 s[8:9], 0
	s_branch .LBB0_213

.LBB0_222:
	s_or_b64 exec, exec, s[4:5]
	s_waitcnt vmcnt(0)
	s_waitcnt vmcnt(0)

.LBB0_240:
	s_or_b64 exec, exec, s[2:3]
	s_mov_b64 s[2:3], exec
	v_mbcnt_lo_u32_b32 v2, s2, 0
	v_mbcnt_hi_u32_b32 v2, s3, v2
	v_cmp_eq_u32_e32 vcc, 0, v2
	s_waitcnt vmcnt(0)
	s_and_saveexec_b64 s[4:5], vcc
	s_cbranch_execz .LBB0_242
	s_bcnt1_i32_b64 s2, s[2:3]
	v_mov_b32_e32 v2, s2
	v_mov_b32_e32 v3, 0x2000
	global_atomic_add v3, v2, s[0:1] offset:1024

.LBB0_348:
	s_or_b64 exec, exec, s[4:5]
	s_mov_b64 s[4:5], exec
	v_mbcnt_lo_u32_b32 v2, s4, 0
	v_mbcnt_hi_u32_b32 v2, s5, v2
	v_cmp_eq_u32_e32 vcc, 0, v2
	s_waitcnt vmcnt(0)
	s_and_saveexec_b64 s[6:7], vcc
	s_cbranch_execz .LBB0_350
	s_bcnt1_i32_b64 s4, s[4:5]
	v_mov_b32_e32 v2, s4
	v_mov_b32_e32 v3, 0x2000
	global_atomic_add v3, v2, s[0:1] offset:1024

.LBB0_752:
	s_or_b64 exec, exec, s[4:5]
	buffer_inv sc1
	s_waitcnt vmcnt(1)
	v_readfirstlane_b32 s2, v5
	v_sub_u32_e32 v6, 0, v4
	s_nop 0
	v_add_u32_e32 v5, s2, v3
	v_cvt_f32_u32_e32 v3, v4
	v_rcp_iflag_f32_e32 v3, v3
	s_nop 0
	v_mul_f32_e32 v3, 0x4f7ffffe, v3
	v_cvt_u32_f32_e32 v3, v3
	v_mul_lo_u32 v6, v6, v3
	v_mul_hi_u32 v6, v3, v6
	v_add_u32_e32 v3, v3, v6
	v_mul_hi_u32 v3, v5, v3
	v_mul_lo_u32 v6, v3, v4
	v_sub_u32_e32 v6, v5, v6
	v_cmp_ge_u32_e32 vcc, v6, v4
	v_add_u32_e32 v7, 1, v3
	s_nop 0
	v_cndmask_b32_e32 v3, v3, v7, vcc
	v_sub_u32_e32 v7, v6, v4
	v_cndmask_b32_e32 v6, v6, v7, vcc
	v_cmp_ge_u32_e32 vcc, v6, v4
	v_add_u32_e32 v6, 1, v3
	s_nop 0
	v_cndmask_b32_e32 v3, v3, v6, vcc
	v_add_u32_e32 v6, 1, v5
	v_mad_u64_u32 v[4:5], s[2:3], v4, v3, v[4:5]
	v_cmp_ne_u32_e32 vcc, v6, v4
	s_and_saveexec_b64 s[2:3], vcc
	s_xor_b64 s[2:3], exec, s[2:3]
	s_cbranch_execz .LBB0_766
	s_waitcnt lgkmcnt(0)
	v_mov_b32_e32 v2, 0x2000
	global_load_dword v2, v2, s[0:1] offset:1024 sc1
	s_add_u32 s6, s0, 0x2400
	s_addc_u32 s7, s1, 0
	s_waitcnt vmcnt(0)
	v_cmp_eq_u32_e32 vcc, v2, v3
	s_and_saveexec_b64 s[4:5], vcc
	s_cbranch_execz .LBB0_765
	s_mov_b32 s18, 1
	s_mov_b64 s[8:9], 0
	s_branch .LBB0_756

.LBB0_1106:
	s_or_b64 exec, exec, s[4:5]
	s_mov_b64 s[4:5], exec
	v_mbcnt_lo_u32_b32 v2, s4, 0
	v_mbcnt_hi_u32_b32 v2, s5, v2
	v_cmp_eq_u32_e32 vcc, 0, v2
	s_waitcnt vmcnt(0)
	s_and_saveexec_b64 s[6:7], vcc
	s_cbranch_execnz .LBB0_1107
	s_getpc_b64 s[98:99]
